# s_setprio 1 over the sparse-attention stage of each query (gather/MFMA/LDS-bound), reset to 0 at the query loop head
# baseline (speedup 1.0000x reference)
.LBB0_701:
	s_setprio 0
	v_readlane_b32 s81, v255, 10
	v_readlane_b32 s16, v255, 14
	v_readlane_b32 s13, v255, 15
	s_add_i32 s16, s16, s81
	s_add_i32 s13, s13, 1
	v_readlane_b32 s96, v255, 11
	s_cmpk_lt_i32 s16, 0x800
	v_readlane_b32 s97, v255, 12
	v_readlane_b32 s12, v255, 13
	s_mov_b64 s[14:15], 0x200
	s_waitcnt lgkmcnt(0)
	s_barrier
	s_cbranch_scc0 .LBB0_1342

.LBB0_716:
	s_setprio 0
	v_mov_b32_e32 v2, 0
	s_and_saveexec_b64 s[0:1], s[4:5]
	s_cbranch_execz .LBB0_720
	s_mov_b64 s[10:11], exec
	v_mbcnt_lo_u32_b32 v2, s10, 0
	v_mbcnt_hi_u32_b32 v2, s11, v2
	v_cmp_eq_u32_e32 vcc, 0, v2
	s_and_saveexec_b64 s[8:9], vcc
	s_cbranch_execz .LBB0_719
	s_bcnt1_i32_b64 s10, s[10:11]
	v_readlane_b32 s11, v255, 7
	s_waitcnt lgkmcnt(0)
	v_mov_b32_e32 v4, s10
	v_mov_b32_e32 v3, s11
	ds_add_rtn_u32 v3, v3, v4

.LBB0_922:
	s_setprio 1
	s_mov_b32 s16, 0
	s_andn2_b64 vcc, exec, s[60:61]
	s_mov_b32 s17, 0
	s_cbranch_vccnz .LBB0_956
	v_cmp_eq_u32_sdwa vcc, v77, v2 src0_sel:WORD_0 src1_sel:DWORD
	v_cmp_eq_u32_sdwa s[10:11], v77, v2 src0_sel:WORD_1 src1_sel:DWORD
	v_cmp_gt_u32_sdwa s[8:9], v77, v2 src0_sel:WORD_0 src1_sel:DWORD
	v_and_b32_e32 v5, vcc_lo, v13
	v_and_b32_e32 v4, vcc_hi, v12
	v_bcnt_u32_b32 v5, v5, 0
	v_and_b32_e32 v6, s10, v13
	v_bcnt_u32_b32 v4, v4, v5
	v_and_b32_e32 v5, s11, v12
	v_bcnt_u32_b32 v6, v6, 0
	v_bcnt_u32_b32 v5, v5, v6
	v_add_u32_e32 v4, v5, v4
	v_addc_co_u32_e64 v5, s[0:1], 0, v4, vcc
	v_cmp_lt_i32_e64 s[0:1], v4, v3
	s_and_b64 s[0:1], vcc, s[0:1]
	s_or_b64 s[16:17], s[8:9], s[0:1]
	v_cmp_lt_i32_e64 s[0:1], v5, v3
	v_cmp_gt_u32_sdwa s[8:9], v77, v2 src0_sel:WORD_1 src1_sel:DWORD
	s_and_b64 s[0:1], s[10:11], s[0:1]
	s_or_b64 s[12:13], s[8:9], s[0:1]
	v_cndmask_b32_e64 v4, 0, 1, s[16:17]
	v_cmp_ne_u32_e64 s[0:1], 0, v4
	v_cndmask_b32_e64 v5, 0, 1, s[12:13]
	v_cmp_ne_u32_e64 s[8:9], 0, v5
	v_and_b32_e32 v6, s0, v13
	v_and_b32_e32 v5, s1, v12
	v_bcnt_u32_b32 v6, v6, 0
	v_and_b32_e32 v7, s8, v13
	v_bcnt_u32_b32 v5, v5, v6
	v_and_b32_e32 v6, s9, v12
	v_bcnt_u32_b32 v7, v7, 0
	v_bcnt_u32_b32 v6, v6, v7
	v_add_u32_e32 v5, v6, v5
	s_and_saveexec_b64 s[14:15], s[16:17]
	v_lshl_add_u32 v6, v5, 1, s95
	ds_write_b16 v6, v11
	s_or_b64 exec, exec, s[14:15]
	s_and_saveexec_b64 s[14:15], s[12:13]
	v_lshlrev_b32_e32 v5, 1, v5
	v_lshlrev_b32_e32 v4, 1, v4
	v_add3_u32 v4, s95, v5, v4
	v_or_b32_e32 v5, 1, v11
	ds_write_b16 v4, v5
	s_or_b64 exec, exec, s[14:15]
	s_bcnt1_i32_b64 s0, s[0:1]
	s_bcnt1_i32_b64 s17, s[8:9]
	s_add_i32 s17, s17, s0
	s_bcnt1_i32_b64 s0, vcc
	s_bcnt1_i32_b64 s16, s[10:11]
	s_add_i32 s16, s16, s0
	v_cmp_eq_u32_sdwa vcc, v76, v2 src0_sel:WORD_0 src1_sel:DWORD
	v_cmp_eq_u32_sdwa s[10:11], v76, v2 src0_sel:WORD_1 src1_sel:DWORD
	v_cmp_gt_u32_sdwa s[8:9], v76, v2 src0_sel:WORD_0 src1_sel:DWORD
	v_and_b32_e32 v5, vcc_lo, v13
	v_and_b32_e32 v4, vcc_hi, v12
	v_bcnt_u32_b32 v5, v5, 0
	v_and_b32_e32 v6, s10, v13
	v_bcnt_u32_b32 v4, v4, v5
	v_and_b32_e32 v5, s11, v12
	v_bcnt_u32_b32 v6, v6, 0
	v_bcnt_u32_b32 v5, v5, v6
	v_add3_u32 v4, s16, v4, v5
	v_addc_co_u32_e64 v5, s[0:1], 0, v4, vcc
	v_cmp_lt_i32_e64 s[0:1], v4, v3
	s_and_b64 s[0:1], vcc, s[0:1]
	s_or_b64 s[18:19], s[8:9], s[0:1]
	v_cmp_lt_i32_e64 s[0:1], v5, v3
	v_cmp_gt_u32_sdwa s[8:9], v76, v2 src0_sel:WORD_1 src1_sel:DWORD
	s_and_b64 s[0:1], s[10:11], s[0:1]
	s_or_b64 s[12:13], s[8:9], s[0:1]
	v_cndmask_b32_e64 v4, 0, 1, s[18:19]
	v_cmp_ne_u32_e64 s[0:1], 0, v4
	v_cndmask_b32_e64 v5, 0, 1, s[12:13]
	v_cmp_ne_u32_e64 s[8:9], 0, v5
	v_and_b32_e32 v6, s0, v13
	v_and_b32_e32 v5, s1, v12
	v_bcnt_u32_b32 v6, v6, 0
	v_and_b32_e32 v7, s8, v13
	v_bcnt_u32_b32 v5, v5, v6
	v_and_b32_e32 v6, s9, v12
	v_bcnt_u32_b32 v7, v7, 0
	v_bcnt_u32_b32 v6, v6, v7
	v_add3_u32 v5, s17, v5, v6
	s_and_saveexec_b64 s[14:15], s[18:19]
	v_lshl_add_u32 v6, v5, 1, s95
	v_add_u16_e32 v7, 0x80, v11
	ds_write_b16 v6, v7
	s_or_b64 exec, exec, s[14:15]
	s_and_saveexec_b64 s[14:15], s[12:13]
	v_lshlrev_b32_e32 v5, 1, v5
	v_lshlrev_b32_e32 v4, 1, v4
	v_add3_u32 v4, s95, v5, v4
	v_add_u16_e32 v5, 0x81, v11
	ds_write_b16 v4, v5
	s_or_b64 exec, exec, s[14:15]
	s_bcnt1_i32_b64 s0, s[0:1]
	s_bcnt1_i32_b64 s1, s[8:9]
	s_add_i32 s17, s17, s0
	s_bcnt1_i32_b64 s0, vcc
	s_add_i32 s17, s17, s1
	s_bcnt1_i32_b64 s1, s[10:11]
	s_add_i32 s16, s16, s0
	s_add_i32 s16, s16, s1
	v_cmp_eq_u32_sdwa vcc, v75, v2 src0_sel:WORD_0 src1_sel:DWORD
	v_cmp_eq_u32_sdwa s[12:13], v75, v2 src0_sel:WORD_1 src1_sel:DWORD
	v_cmp_gt_u32_sdwa s[8:9], v75, v2 src0_sel:WORD_0 src1_sel:DWORD
	v_and_b32_e32 v5, vcc_lo, v13
	v_and_b32_e32 v4, vcc_hi, v12
	v_bcnt_u32_b32 v5, v5, 0
	v_and_b32_e32 v6, s12, v13
	v_bcnt_u32_b32 v4, v4, v5
	v_and_b32_e32 v5, s13, v12
	v_bcnt_u32_b32 v6, v6, 0
	v_bcnt_u32_b32 v5, v5, v6
	v_add3_u32 v4, s16, v4, v5
	v_addc_co_u32_e64 v5, s[0:1], 0, v4, vcc
	v_cmp_lt_i32_e64 s[0:1], v4, v3
	s_and_b64 s[10:11], vcc, s[0:1]
	v_cmp_lt_i32_e64 s[0:1], v5, v3
	v_cmp_gt_u32_sdwa s[14:15], v75, v2 src0_sel:WORD_1 src1_sel:DWORD
	s_and_b64 s[18:19], s[12:13], s[0:1]
	s_or_b64 s[20:21], s[8:9], s[10:11]
	v_cndmask_b32_e64 v4, 0, 1, s[20:21]
	s_or_b64 s[14:15], s[14:15], s[18:19]
	v_cmp_ne_u32_e64 s[0:1], 0, v4
	v_cndmask_b32_e64 v5, 0, 1, s[14:15]
	v_cmp_ne_u32_e64 s[8:9], 0, v5
	v_and_b32_e32 v6, s0, v13
	v_and_b32_e32 v5, s1, v12
	v_bcnt_u32_b32 v6, v6, 0
	v_and_b32_e32 v7, s8, v13
	v_bcnt_u32_b32 v5, v5, v6
	v_and_b32_e32 v6, s9, v12
	v_bcnt_u32_b32 v7, v7, 0
	v_bcnt_u32_b32 v6, v6, v7
	v_add3_u32 v5, s17, v5, v6
	v_cmp_gt_u32_e64 s[10:11], s80, v5
	s_and_b64 s[18:19], s[20:21], s[10:11]
	s_and_saveexec_b64 s[10:11], s[18:19]
	v_lshl_add_u32 v6, v5, 1, s95
	v_add_u16_e32 v7, 0x100, v11
	ds_write_b16 v6, v7
	s_or_b64 exec, exec, s[10:11]
	v_add_u32_e32 v4, v5, v4
	v_cmp_gt_u32_e64 s[10:11], s80, v4
	s_and_b64 s[14:15], s[14:15], s[10:11]
	s_and_saveexec_b64 s[10:11], s[14:15]
	v_lshl_add_u32 v4, v4, 1, s95
	v_add_u16_e32 v5, 0x101, v11
	ds_write_b16 v4, v5
	s_or_b64 exec, exec, s[10:11]
	s_bcnt1_i32_b64 s0, s[0:1]
	s_bcnt1_i32_b64 s1, s[8:9]
	s_add_i32 s17, s17, s0
	s_bcnt1_i32_b64 s0, vcc
	s_add_i32 s17, s17, s1
	s_bcnt1_i32_b64 s1, s[12:13]
	s_add_i32 s16, s16, s0
	s_add_i32 s16, s16, s1
	v_cmp_eq_u32_sdwa vcc, v74, v2 src0_sel:WORD_0 src1_sel:DWORD
	v_cmp_eq_u32_sdwa s[12:13], v74, v2 src0_sel:WORD_1 src1_sel:DWORD
	v_cmp_gt_u32_sdwa s[8:9], v74, v2 src0_sel:WORD_0 src1_sel:DWORD
	v_and_b32_e32 v5, vcc_lo, v13
	v_and_b32_e32 v4, vcc_hi, v12
	v_bcnt_u32_b32 v5, v5, 0
	v_and_b32_e32 v6, s12, v13
	v_bcnt_u32_b32 v4, v4, v5
	v_and_b32_e32 v5, s13, v12
	v_bcnt_u32_b32 v6, v6, 0
	v_bcnt_u32_b32 v5, v5, v6
	v_add3_u32 v4, s16, v4, v5
	v_addc_co_u32_e64 v5, s[0:1], 0, v4, vcc
	v_cmp_lt_i32_e64 s[0:1], v4, v3
	s_and_b64 s[10:11], vcc, s[0:1]
	v_cmp_lt_i32_e64 s[0:1], v5, v3
	v_cmp_gt_u32_sdwa s[14:15], v74, v2 src0_sel:WORD_1 src1_sel:DWORD
	s_and_b64 s[18:19], s[12:13], s[0:1]
	s_or_b64 s[20:21], s[8:9], s[10:11]
	v_cndmask_b32_e64 v4, 0, 1, s[20:21]
	s_or_b64 s[14:15], s[14:15], s[18:19]
	v_cmp_ne_u32_e64 s[0:1], 0, v4
	v_cndmask_b32_e64 v5, 0, 1, s[14:15]
	v_cmp_ne_u32_e64 s[8:9], 0, v5
	v_and_b32_e32 v6, s0, v13
	v_and_b32_e32 v5, s1, v12
	v_bcnt_u32_b32 v6, v6, 0
	v_and_b32_e32 v7, s8, v13
	v_bcnt_u32_b32 v5, v5, v6
	v_and_b32_e32 v6, s9, v12
	v_bcnt_u32_b32 v7, v7, 0
	v_bcnt_u32_b32 v6, v6, v7
	v_add3_u32 v5, s17, v5, v6
	v_cmp_gt_u32_e64 s[10:11], s80, v5
	s_and_b64 s[18:19], s[20:21], s[10:11]
	s_and_saveexec_b64 s[10:11], s[18:19]
	v_lshl_add_u32 v6, v5, 1, s95
	v_add_u16_e32 v7, 0x180, v11
	ds_write_b16 v6, v7
	s_or_b64 exec, exec, s[10:11]
	v_add_u32_e32 v4, v5, v4
	v_cmp_gt_u32_e64 s[10:11], s80, v4
	s_and_b64 s[14:15], s[14:15], s[10:11]
	s_and_saveexec_b64 s[10:11], s[14:15]
	v_lshl_add_u32 v4, v4, 1, s95
	v_add_u16_e32 v5, 0x181, v11
	ds_write_b16 v4, v5
	s_or_b64 exec, exec, s[10:11]
	s_bcnt1_i32_b64 s0, s[0:1]
	s_bcnt1_i32_b64 s1, s[8:9]
	s_add_i32 s17, s17, s0
	s_bcnt1_i32_b64 s0, vcc
	s_add_i32 s17, s17, s1
	s_bcnt1_i32_b64 s1, s[12:13]
	s_add_i32 s16, s16, s0
	s_add_i32 s16, s16, s1
	v_cmp_eq_u32_sdwa vcc, v73, v2 src0_sel:WORD_0 src1_sel:DWORD
	v_cmp_eq_u32_sdwa s[12:13], v73, v2 src0_sel:WORD_1 src1_sel:DWORD
	v_cmp_gt_u32_sdwa s[8:9], v73, v2 src0_sel:WORD_0 src1_sel:DWORD
	v_and_b32_e32 v5, vcc_lo, v13
	v_and_b32_e32 v4, vcc_hi, v12
	v_bcnt_u32_b32 v5, v5, 0
	v_and_b32_e32 v6, s12, v13
	v_bcnt_u32_b32 v4, v4, v5
	v_and_b32_e32 v5, s13, v12
	v_bcnt_u32_b32 v6, v6, 0
	v_bcnt_u32_b32 v5, v5, v6
	v_add3_u32 v4, s16, v4, v5
	v_addc_co_u32_e64 v5, s[0:1], 0, v4, vcc
	v_cmp_lt_i32_e64 s[0:1], v4, v3
	s_and_b64 s[10:11], vcc, s[0:1]
	v_cmp_lt_i32_e64 s[0:1], v5, v3
	v_cmp_gt_u32_sdwa s[14:15], v73, v2 src0_sel:WORD_1 src1_sel:DWORD
	s_and_b64 s[18:19], s[12:13], s[0:1]
	s_or_b64 s[20:21], s[8:9], s[10:11]
	v_cndmask_b32_e64 v4, 0, 1, s[20:21]
	s_or_b64 s[14:15], s[14:15], s[18:19]
	v_cmp_ne_u32_e64 s[0:1], 0, v4
	v_cndmask_b32_e64 v5, 0, 1, s[14:15]
	v_cmp_ne_u32_e64 s[8:9], 0, v5
	v_and_b32_e32 v6, s0, v13
	v_and_b32_e32 v5, s1, v12
	v_bcnt_u32_b32 v6, v6, 0
	v_and_b32_e32 v7, s8, v13
	v_bcnt_u32_b32 v5, v5, v6
	v_and_b32_e32 v6, s9, v12
	v_bcnt_u32_b32 v7, v7, 0
	v_bcnt_u32_b32 v6, v6, v7
	v_add3_u32 v5, s17, v5, v6
	v_cmp_gt_u32_e64 s[10:11], s80, v5
	s_and_b64 s[18:19], s[20:21], s[10:11]
	s_and_saveexec_b64 s[10:11], s[18:19]
	v_lshl_add_u32 v6, v5, 1, s95
	v_add_u16_e32 v7, 0x200, v11
	ds_write_b16 v6, v7
	s_or_b64 exec, exec, s[10:11]
	v_add_u32_e32 v4, v5, v4
	v_cmp_gt_u32_e64 s[10:11], s80, v4
	s_and_b64 s[14:15], s[14:15], s[10:11]
	s_and_saveexec_b64 s[10:11], s[14:15]
	v_lshl_add_u32 v4, v4, 1, s95
	v_add_u16_e32 v5, 0x201, v11
	ds_write_b16 v4, v5
	s_or_b64 exec, exec, s[10:11]
	s_bcnt1_i32_b64 s0, s[0:1]
	s_bcnt1_i32_b64 s1, s[8:9]
	s_add_i32 s17, s17, s0
	s_bcnt1_i32_b64 s0, vcc
	s_add_i32 s17, s17, s1
	s_bcnt1_i32_b64 s1, s[12:13]
	s_add_i32 s16, s16, s0
	s_add_i32 s16, s16, s1
	v_cmp_eq_u32_sdwa vcc, v72, v2 src0_sel:WORD_0 src1_sel:DWORD
	v_cmp_eq_u32_sdwa s[12:13], v72, v2 src0_sel:WORD_1 src1_sel:DWORD
	v_cmp_gt_u32_sdwa s[8:9], v72, v2 src0_sel:WORD_0 src1_sel:DWORD
	v_and_b32_e32 v5, vcc_lo, v13
	v_and_b32_e32 v4, vcc_hi, v12
	v_bcnt_u32_b32 v5, v5, 0
	v_and_b32_e32 v6, s12, v13
	v_bcnt_u32_b32 v4, v4, v5
	v_and_b32_e32 v5, s13, v12
	v_bcnt_u32_b32 v6, v6, 0
	v_bcnt_u32_b32 v5, v5, v6
	v_add3_u32 v4, s16, v4, v5
	v_addc_co_u32_e64 v5, s[0:1], 0, v4, vcc
	v_cmp_lt_i32_e64 s[0:1], v4, v3
	s_and_b64 s[10:11], vcc, s[0:1]
	v_cmp_lt_i32_e64 s[0:1], v5, v3
	v_cmp_gt_u32_sdwa s[14:15], v72, v2 src0_sel:WORD_1 src1_sel:DWORD
	s_and_b64 s[18:19], s[12:13], s[0:1]
	s_or_b64 s[20:21], s[8:9], s[10:11]
	v_cndmask_b32_e64 v4, 0, 1, s[20:21]
	s_or_b64 s[14:15], s[14:15], s[18:19]
	v_cmp_ne_u32_e64 s[0:1], 0, v4
	v_cndmask_b32_e64 v5, 0, 1, s[14:15]
	v_cmp_ne_u32_e64 s[8:9], 0, v5
	v_and_b32_e32 v6, s0, v13
	v_and_b32_e32 v5, s1, v12
	v_bcnt_u32_b32 v6, v6, 0
	v_and_b32_e32 v7, s8, v13
	v_bcnt_u32_b32 v5, v5, v6
	v_and_b32_e32 v6, s9, v12
	v_bcnt_u32_b32 v7, v7, 0
	v_bcnt_u32_b32 v6, v6, v7
	v_add3_u32 v5, s17, v5, v6
	v_cmp_gt_u32_e64 s[10:11], s80, v5
	s_and_b64 s[18:19], s[20:21], s[10:11]
	s_and_saveexec_b64 s[10:11], s[18:19]
	v_lshl_add_u32 v6, v5, 1, s95
	v_add_u16_e32 v7, 0x280, v11
	ds_write_b16 v6, v7
	s_or_b64 exec, exec, s[10:11]
	v_add_u32_e32 v4, v5, v4
	v_cmp_gt_u32_e64 s[10:11], s80, v4
	s_and_b64 s[14:15], s[14:15], s[10:11]
	s_and_saveexec_b64 s[10:11], s[14:15]
	v_lshl_add_u32 v4, v4, 1, s95
	v_add_u16_e32 v5, 0x281, v11
	ds_write_b16 v4, v5
	s_or_b64 exec, exec, s[10:11]
	s_bcnt1_i32_b64 s0, s[0:1]
	s_bcnt1_i32_b64 s1, s[8:9]
	s_add_i32 s17, s17, s0
	s_bcnt1_i32_b64 s0, vcc
	s_add_i32 s17, s17, s1
	s_bcnt1_i32_b64 s1, s[12:13]
	s_add_i32 s16, s16, s0
	s_add_i32 s16, s16, s1
	v_cmp_eq_u32_sdwa vcc, v71, v2 src0_sel:WORD_0 src1_sel:DWORD
	v_cmp_eq_u32_sdwa s[12:13], v71, v2 src0_sel:WORD_1 src1_sel:DWORD
	v_cmp_gt_u32_sdwa s[8:9], v71, v2 src0_sel:WORD_0 src1_sel:DWORD
	v_and_b32_e32 v5, vcc_lo, v13
	v_and_b32_e32 v4, vcc_hi, v12
	v_bcnt_u32_b32 v5, v5, 0
	v_and_b32_e32 v6, s12, v13
	v_bcnt_u32_b32 v4, v4, v5
	v_and_b32_e32 v5, s13, v12
	v_bcnt_u32_b32 v6, v6, 0
	v_bcnt_u32_b32 v5, v5, v6
	v_add3_u32 v4, s16, v4, v5
	v_addc_co_u32_e64 v5, s[0:1], 0, v4, vcc
	v_cmp_lt_i32_e64 s[0:1], v4, v3
	s_and_b64 s[10:11], vcc, s[0:1]
	v_cmp_lt_i32_e64 s[0:1], v5, v3
	v_cmp_gt_u32_sdwa s[14:15], v71, v2 src0_sel:WORD_1 src1_sel:DWORD
	s_and_b64 s[18:19], s[12:13], s[0:1]
	s_or_b64 s[20:21], s[8:9], s[10:11]
	v_cndmask_b32_e64 v4, 0, 1, s[20:21]
	s_or_b64 s[14:15], s[14:15], s[18:19]
	v_cmp_ne_u32_e64 s[0:1], 0, v4
	v_cndmask_b32_e64 v5, 0, 1, s[14:15]
	v_cmp_ne_u32_e64 s[8:9], 0, v5
	v_and_b32_e32 v6, s0, v13
	v_and_b32_e32 v5, s1, v12
	v_bcnt_u32_b32 v6, v6, 0
	v_and_b32_e32 v7, s8, v13
	v_bcnt_u32_b32 v5, v5, v6
	v_and_b32_e32 v6, s9, v12
	v_bcnt_u32_b32 v7, v7, 0
	v_bcnt_u32_b32 v6, v6, v7
	v_add3_u32 v5, s17, v5, v6
	v_cmp_gt_u32_e64 s[10:11], s80, v5
	s_and_b64 s[18:19], s[20:21], s[10:11]
	s_and_saveexec_b64 s[10:11], s[18:19]
	v_lshl_add_u32 v6, v5, 1, s95
	v_add_u16_e32 v7, 0x300, v11
	ds_write_b16 v6, v7
	s_or_b64 exec, exec, s[10:11]
	v_add_u32_e32 v4, v5, v4
	v_cmp_gt_u32_e64 s[10:11], s80, v4
	s_and_b64 s[14:15], s[14:15], s[10:11]
	s_and_saveexec_b64 s[10:11], s[14:15]
	v_lshl_add_u32 v4, v4, 1, s95
	v_add_u16_e32 v5, 0x301, v11
	ds_write_b16 v4, v5
	s_or_b64 exec, exec, s[10:11]
	s_bcnt1_i32_b64 s0, s[0:1]
	s_bcnt1_i32_b64 s1, s[8:9]
	s_add_i32 s17, s17, s0
	s_bcnt1_i32_b64 s0, vcc
	s_add_i32 s17, s17, s1
	s_bcnt1_i32_b64 s1, s[12:13]
	s_add_i32 s16, s16, s0
	s_add_i32 s16, s16, s1
	v_cmp_eq_u32_sdwa vcc, v70, v2 src0_sel:WORD_0 src1_sel:DWORD
	v_cmp_eq_u32_sdwa s[12:13], v70, v2 src0_sel:WORD_1 src1_sel:DWORD
	v_cmp_gt_u32_sdwa s[8:9], v70, v2 src0_sel:WORD_0 src1_sel:DWORD
	v_and_b32_e32 v5, vcc_lo, v13
	v_and_b32_e32 v4, vcc_hi, v12
	v_bcnt_u32_b32 v5, v5, 0
	v_and_b32_e32 v6, s12, v13
	v_bcnt_u32_b32 v4, v4, v5
	v_and_b32_e32 v5, s13, v12
	v_bcnt_u32_b32 v6, v6, 0
	v_bcnt_u32_b32 v5, v5, v6
	v_add3_u32 v4, s16, v4, v5
	v_addc_co_u32_e64 v5, s[0:1], 0, v4, vcc
	v_cmp_lt_i32_e64 s[0:1], v4, v3
	s_and_b64 s[10:11], vcc, s[0:1]
	v_cmp_lt_i32_e64 s[0:1], v5, v3
	v_cmp_gt_u32_sdwa s[14:15], v70, v2 src0_sel:WORD_1 src1_sel:DWORD
	s_and_b64 s[18:19], s[12:13], s[0:1]
	s_or_b64 s[20:21], s[8:9], s[10:11]
	v_cndmask_b32_e64 v4, 0, 1, s[20:21]
	s_or_b64 s[14:15], s[14:15], s[18:19]
	v_cmp_ne_u32_e64 s[0:1], 0, v4
	v_cndmask_b32_e64 v5, 0, 1, s[14:15]
	v_cmp_ne_u32_e64 s[8:9], 0, v5
	v_and_b32_e32 v6, s0, v13
	v_and_b32_e32 v5, s1, v12
	v_bcnt_u32_b32 v6, v6, 0
	v_and_b32_e32 v7, s8, v13
	v_bcnt_u32_b32 v5, v5, v6
	v_and_b32_e32 v6, s9, v12
	v_bcnt_u32_b32 v7, v7, 0
	v_bcnt_u32_b32 v6, v6, v7
	v_add3_u32 v5, s17, v5, v6
	v_cmp_gt_u32_e64 s[10:11], s80, v5
	s_and_b64 s[18:19], s[20:21], s[10:11]
	s_and_saveexec_b64 s[10:11], s[18:19]
	v_lshl_add_u32 v6, v5, 1, s95
	v_add_u16_e32 v7, 0x380, v11
	ds_write_b16 v6, v7
	s_or_b64 exec, exec, s[10:11]
	v_add_u32_e32 v4, v5, v4
	v_cmp_gt_u32_e64 s[10:11], s80, v4
	s_and_b64 s[14:15], s[14:15], s[10:11]
	s_and_saveexec_b64 s[10:11], s[14:15]
	v_lshl_add_u32 v4, v4, 1, s95
	v_add_u16_e32 v5, 0x381, v11
	ds_write_b16 v4, v5
	s_or_b64 exec, exec, s[10:11]
	s_bcnt1_i32_b64 s0, s[0:1]
	s_bcnt1_i32_b64 s1, s[8:9]
	s_add_i32 s0, s17, s0
	s_add_i32 s17, s0, s1
	s_bcnt1_i32_b64 s0, vcc
	s_bcnt1_i32_b64 s1, s[12:13]
	s_add_i32 s0, s16, s0
	s_add_i32 s16, s0, s1
